# speedup vs baseline: 1.0345x; 1.0146x over previous
.LBB3_1:
	s_waitcnt vmcnt(3) lgkmcnt(0)
	s_barrier
	s_add_u32 s34, s20, s28
	s_addc_u32 s35, s21, s27
	s_add_i32 s31, s30, s23
	s_mov_b32 s36, m0
	s_mov_b32 m0, s31
	s_nop 0
	global_load_lds_dwordx4 v100, s[14:15]
	s_mov_b32 m0, s36
	s_addk_i32 s31, 0x400
	s_mov_b32 s36, m0
	s_mov_b32 m0, s31
	s_nop 0
	global_load_lds_dwordx4 v99, s[14:15]
	s_mov_b32 m0, s36
	s_waitcnt lgkmcnt(3)
	v_mfma_f32_16x16x32_f16 v[92:95], v[20:23], v[28:31], v[92:95]
	s_add_i32 s33, s30, s26
	s_mov_b32 s31, m0
	s_mov_b32 m0, s33
	s_nop 0
	global_load_lds_dwordx4 v102, s[34:35]
	s_mov_b32 m0, s31
	s_addk_i32 s30, 0x6000
	v_mfma_f32_16x16x32_f16 v[72:75], v[20:23], v[24:27], v[72:75]
	v_mfma_f32_16x16x32_f16 v[56:59], v[20:23], v[16:19], v[56:59]
	v_mfma_f32_16x16x32_f16 v[20:23], v[20:23], v[0:3], v[40:43]
	s_nop 2
	v_add_u32_e32 v41, s29, v103
	s_waitcnt lgkmcnt(2)
	v_mfma_f32_16x16x32_f16 v[88:91], v[12:15], v[28:31], v[88:91]
	v_add_u32_e32 v40, s29, v98
	s_addk_i32 s29, 0x6000
	s_cmp_lg_u32 s30, 0x18000
	s_waitcnt lgkmcnt(1)
	v_mfma_f32_16x16x32_f16 v[80:83], v[8:11], v[28:31], v[80:83]
	s_cselect_b32 s33, s30, 0
	s_cmp_lg_u32 s29, 0x18000
	s_cselect_b32 s29, s29, 0
	s_waitcnt lgkmcnt(0)
	v_mfma_f32_16x16x32_f16 v[28:31], v[4:7], v[28:31], v[76:79]
	s_add_u32 s30, s14, 0x80000
	s_addc_u32 s31, s15, 0
	s_add_u32 s34, s20, s18
	v_mfma_f32_16x16x32_f16 v[68:71], v[12:15], v[24:27], v[68:71]
	s_addc_u32 s35, s21, s19
	s_add_i32 s36, s33, s23
	v_add_u32_e32 v116, s29, v98
	v_mfma_f32_16x16x32_f16 v[64:67], v[8:11], v[24:27], v[64:67]
	v_add_u32_e32 v117, s29, v103
	s_add_i32 s37, s33, s26
	s_addk_i32 s33, 0x6000
	v_mfma_f32_16x16x32_f16 v[24:27], v[4:7], v[24:27], v[60:63]
	s_addk_i32 s29, 0x6000
	v_mfma_f32_16x16x32_f16 v[48:51], v[12:15], v[16:19], v[48:51]
	v_mfma_f32_16x16x32_f16 v[52:55], v[8:11], v[16:19], v[52:55]
	v_mfma_f32_16x16x32_f16 v[16:19], v[4:7], v[16:19], v[44:47]
	v_mfma_f32_16x16x32_f16 v[36:39], v[12:15], v[0:3], v[36:39]
	v_mfma_f32_16x16x32_f16 v[32:35], v[8:11], v[0:3], v[32:35]
	v_mfma_f32_16x16x32_f16 v[84:87], v[4:7], v[0:3], v[84:87]
	ds_read_b128 v[0:3], v41 offset:16384
	ds_read_b128 v[4:7], v41 offset:17408
	ds_read_b128 v[8:11], v40
	ds_read_b128 v[12:15], v40 offset:1024
	ds_read_b128 v[104:107], v41 offset:18432
	ds_read_b128 v[108:111], v41 offset:19456
	s_waitcnt lgkmcnt(3)
	v_mfma_f32_16x16x32_f16 v[92:95], v[0:3], v[8:11], v[92:95]
	v_mfma_f32_16x16x32_f16 v[88:91], v[4:7], v[8:11], v[88:91]
	s_waitcnt lgkmcnt(1)
	v_mfma_f32_16x16x32_f16 v[80:83], v[104:107], v[8:11], v[80:83]
	s_waitcnt lgkmcnt(0)
	v_mfma_f32_16x16x32_f16 v[76:79], v[108:111], v[8:11], v[28:31]
	ds_read_b128 v[8:11], v40 offset:2048
	ds_read_b128 v[112:115], v40 offset:3072
	s_waitcnt vmcnt(3) lgkmcnt(0)
	s_barrier
	s_mov_b32 s38, m0
	s_mov_b32 m0, s36
	s_nop 0
	global_load_lds_dwordx4 v100, s[30:31]
	s_mov_b32 m0, s38
	s_addk_i32 s36, 0x400
	s_mov_b32 s38, m0
	s_mov_b32 m0, s36
	s_nop 0
	global_load_lds_dwordx4 v99, s[30:31]
	s_mov_b32 m0, s38
	s_cmp_lg_u32 s33, 0x18000
	s_mov_b32 s30, m0
	s_mov_b32 m0, s37
	s_nop 0
	global_load_lds_dwordx4 v102, s[34:35]
	s_mov_b32 m0, s30
	s_cselect_b32 s30, s33, 0
	s_cmp_lg_u32 s29, 0x18000
	v_mfma_f32_16x16x32_f16 v[72:75], v[0:3], v[12:15], v[72:75]
	s_cselect_b32 s29, s29, 0
	s_add_i32 s13, s13, 2
	s_add_u32 s14, s14, 0x100000
	v_mfma_f32_16x16x32_f16 v[68:71], v[4:7], v[12:15], v[68:71]
	s_addc_u32 s15, s15, 0
	s_add_u32 s20, s20, s16
	s_addc_u32 s21, s21, s17
	v_mfma_f32_16x16x32_f16 v[64:67], v[104:107], v[12:15], v[64:67]
	s_cmp_gt_u32 s13, 25
	v_mfma_f32_16x16x32_f16 v[60:63], v[108:111], v[12:15], v[24:27]
	s_waitcnt lgkmcnt(1)
	v_mfma_f32_16x16x32_f16 v[56:59], v[0:3], v[8:11], v[56:59]
	v_mfma_f32_16x16x32_f16 v[44:47], v[108:111], v[8:11], v[16:19]
	ds_read_b128 v[28:31], v116
	ds_read_b128 v[24:27], v116 offset:1024
	s_nop 0
	ds_read_b128 v[16:19], v116 offset:2048
	s_waitcnt lgkmcnt(3)
	v_mfma_f32_16x16x32_f16 v[40:43], v[0:3], v[112:115], v[20:23]
	ds_read_b128 v[0:3], v116 offset:3072
	s_nop 1
	ds_read_b128 v[20:23], v117 offset:16384
	ds_read_b128 v[12:15], v117 offset:17408
	v_mfma_f32_16x16x32_f16 v[48:51], v[4:7], v[8:11], v[48:51]
	v_mfma_f32_16x16x32_f16 v[52:55], v[104:107], v[8:11], v[52:55]
	v_mfma_f32_16x16x32_f16 v[36:39], v[4:7], v[112:115], v[36:39]
	ds_read_b128 v[8:11], v117 offset:18432
	ds_read_b128 v[4:7], v117 offset:19456
	v_mfma_f32_16x16x32_f16 v[32:35], v[104:107], v[112:115], v[32:35]
	v_mfma_f32_16x16x32_f16 v[84:87], v[108:111], v[112:115], v[84:87]
	s_cbranch_scc0 .LBB3_1
	s_lshl_b32 s13, s24, 8
	s_add_u32 s4, s4, 0xf80000
	s_addc_u32 s5, s5, 0
	s_mul_i32 s15, s12, 0x7c0
	s_waitcnt vmcnt(3) lgkmcnt(0)
	s_barrier
	s_mul_hi_i32 s14, s12, 0x7c0
	s_add_u32 s6, s6, s15
	s_addc_u32 s7, s7, s14
	s_add_i32 s14, s23, 0x12000
	s_mov_b32 s15, m0
	s_mov_b32 m0, s14
	s_nop 0
	global_load_lds_dwordx4 v100, s[4:5]
	s_mov_b32 m0, s15
	s_add_i32 s23, s23, 0x12400
	s_mov_b32 s14, m0
	s_mov_b32 m0, s23
	s_nop 0
	global_load_lds_dwordx4 v99, s[4:5]
	s_mov_b32 m0, s14
	s_add_i32 s25, s25, 0x16000
	s_mov_b32 s4, m0
	s_mov_b32 m0, s25
	s_nop 0
	global_load_lds_dwordx4 v102, s[6:7]
	s_mov_b32 m0, s4
	s_waitcnt lgkmcnt(3)
	v_mfma_f32_16x16x32_f16 v[92:95], v[20:23], v[28:31], v[92:95]
	v_lshlrev_b32_e32 v97, 3, v97
	v_and_or_b32 v97, v97, 24, s22
	v_or_b32_e32 v126, s2, v97
	s_waitcnt lgkmcnt(2)
	v_mfma_f32_16x16x32_f16 v[88:91], v[12:15], v[28:31], v[88:91]
	v_ashrrev_i32_e32 v127, 31, v126
	v_add_u32_e32 v99, 0x12400, v101
	v_add_u32_e32 v122, 0x12c00, v101
	s_waitcnt lgkmcnt(1)
	v_mfma_f32_16x16x32_f16 v[80:83], v[8:11], v[28:31], v[80:83]
	v_lshlrev_b64 v[138:139], 2, v[126:127]
	v_lshl_add_u64 v[134:135], s[10:11], 0, v[138:139]
	s_load_dword s0, s[0:1], 0x2c
	s_waitcnt lgkmcnt(0)
	v_mfma_f32_16x16x32_f16 v[28:31], v[4:7], v[28:31], v[76:79]
	s_add_i32 s3, s3, s13
	v_or_b32_e32 v140, s3, v96
	v_mad_i64_i32 v[96:97], s[2:3], v140, s12, 0
	v_mfma_f32_16x16x32_f16 v[72:75], v[20:23], v[24:27], v[72:75]
	v_lshl_add_u64 v[96:97], v[96:97], 2, s[8:9]
	v_lshl_add_u64 v[96:97], v[96:97], 0, v[138:139]
	v_mfma_f32_16x16x32_f16 v[68:71], v[12:15], v[24:27], v[68:71]
	v_mfma_f32_16x16x32_f16 v[64:67], v[8:11], v[24:27], v[64:67]
	v_mfma_f32_16x16x32_f16 v[24:27], v[4:7], v[24:27], v[60:63]
	v_mfma_f32_16x16x32_f16 v[56:59], v[20:23], v[16:19], v[56:59]
	v_mfma_f32_16x16x32_f16 v[48:51], v[12:15], v[16:19], v[48:51]
	v_mfma_f32_16x16x32_f16 v[52:55], v[8:11], v[16:19], v[52:55]
	v_mfma_f32_16x16x32_f16 v[16:19], v[4:7], v[16:19], v[44:47]
	v_mfma_f32_16x16x32_f16 v[20:23], v[20:23], v[0:3], v[40:43]
	v_mfma_f32_16x16x32_f16 v[12:15], v[12:15], v[0:3], v[36:39]
	v_mfma_f32_16x16x32_f16 v[8:11], v[8:11], v[0:3], v[32:35]
	s_nop 2
	ds_read_b128 v[32:35], v103 offset:40960
	ds_read_b128 v[36:39], v103 offset:41984
	v_mfma_f32_16x16x32_f16 v[0:3], v[4:7], v[0:3], v[84:87]
	ds_read_b128 v[4:7], v98 offset:24576
	ds_read_b128 v[40:43], v98 offset:25600
	ds_read_b128 v[60:63], v103 offset:43008
	ds_read_b128 v[84:87], v103 offset:44032
	s_waitcnt lgkmcnt(3)
	v_mfma_f32_16x16x32_f16 v[44:47], v[32:35], v[4:7], v[92:95]
	v_mfma_f32_16x16x32_f16 v[76:79], v[36:39], v[4:7], v[88:91]
	s_waitcnt lgkmcnt(1)
	v_mfma_f32_16x16x32_f16 v[80:83], v[60:63], v[4:7], v[80:83]
	s_waitcnt lgkmcnt(0)
	v_mfma_f32_16x16x32_f16 v[28:31], v[84:87], v[4:7], v[28:31]
	v_mfma_f32_16x16x32_f16 v[72:75], v[32:35], v[40:43], v[72:75]
	v_mfma_f32_16x16x32_f16 v[68:71], v[36:39], v[40:43], v[68:71]
	v_mfma_f32_16x16x32_f16 v[64:67], v[60:63], v[40:43], v[64:67]
	v_mfma_f32_16x16x32_f16 v[24:27], v[84:87], v[40:43], v[24:27]
	ds_read_b128 v[4:7], v98 offset:26624
	ds_read_b128 v[40:43], v98 offset:27648
	s_waitcnt vmcnt(3) lgkmcnt(0)
	s_barrier
	s_waitcnt lgkmcnt(1)
	v_mfma_f32_16x16x32_f16 v[56:59], v[32:35], v[4:7], v[56:59]
	s_waitcnt lgkmcnt(0)
	v_mfma_f32_16x16x32_f16 v[20:23], v[32:35], v[40:43], v[20:23]
	ds_read_b128 v[32:35], v101 offset:49152
	v_mfma_f32_16x16x32_f16 v[48:51], v[36:39], v[4:7], v[48:51]
	v_mfma_f32_16x16x32_f16 v[52:55], v[60:63], v[4:7], v[52:55]
	v_mfma_f32_16x16x32_f16 v[16:19], v[84:87], v[4:7], v[16:19]
	v_mfma_f32_16x16x32_f16 v[12:15], v[36:39], v[40:43], v[12:15]
	v_mfma_f32_16x16x32_f16 v[36:39], v[60:63], v[40:43], v[8:11]
	ds_read_b128 v[60:63], v98 offset:49152
	ds_read_b128 v[88:91], v98 offset:50176
	ds_read_b128 v[92:95], v101 offset:50176
	v_mfma_f32_16x16x32_f16 v[4:7], v[84:87], v[40:43], v[0:3]
	ds_read_b128 v[40:43], v98 offset:51200
	ds_read_b128 v[8:11], v98 offset:52224
	ds_read_b128 v[84:87], v101 offset:51200
	ds_read_b128 v[102:105], v101 offset:52224
	s_waitcnt vmcnt(0) lgkmcnt(0)
	s_barrier
	v_add_u32_e32 v0, 0x12000, v98
	v_add_u32_e32 v1, 0x12400, v98
	ds_read_b128 v[106:109], v0
	ds_read_b128 v[110:113], v1
	v_add_u32_e32 v0, 0x12800, v98
	v_add_u32_e32 v1, 0x12c00, v98
	v_add_u32_e32 v98, 0x12000, v101
	s_waitcnt lgkmcnt(8)
	v_mfma_f32_16x16x32_f16 v[44:47], v[32:35], v[60:63], v[44:47]
	ds_read_b128 v[114:117], v0
	ds_read_b128 v[0:3], v1
	s_waitcnt lgkmcnt(8)
	v_mfma_f32_16x16x32_f16 v[76:79], v[92:95], v[60:63], v[76:79]
	s_waitcnt lgkmcnt(5)
	v_mfma_f32_16x16x32_f16 v[80:83], v[84:87], v[60:63], v[80:83]
	s_waitcnt lgkmcnt(4)
	v_mfma_f32_16x16x32_f16 v[28:31], v[102:105], v[60:63], v[28:31]
	ds_read_b128 v[60:63], v98
	ds_read_b128 v[118:121], v99
	v_add_u32_e32 v98, 0x12800, v101
	ds_read_b128 v[98:101], v98
	ds_read_b128 v[122:125], v122
	s_waitcnt vmcnt(0) lgkmcnt(0)
	s_barrier
	global_load_dwordx4 v[148:151], v[134:135], off
	global_load_dwordx4 v[152:155], v[134:135], off offset:16
	global_load_dwordx4 v[156:159], v[134:135], off offset:128
	global_load_dwordx4 v[160:163], v[134:135], off offset:144
	v_and_b32_e32 v141, 24, v126
	v_lshlrev_b32_e32 v141, 1, v141
	v_sub_u32_e32 v138, v138, v141
	v_mfma_f32_16x16x32_f16 v[72:75], v[32:35], v[88:91], v[72:75]
	v_mfma_f32_16x16x32_f16 v[68:71], v[92:95], v[88:91], v[68:71]
	v_mfma_f32_16x16x32_f16 v[64:67], v[84:87], v[88:91], v[64:67]
	v_mfma_f32_16x16x32_f16 v[24:27], v[102:105], v[88:91], v[24:27]
	v_mfma_f32_16x16x32_f16 v[56:59], v[32:35], v[40:43], v[56:59]
	v_mfma_f32_16x16x32_f16 v[48:51], v[92:95], v[40:43], v[48:51]
	v_mfma_f32_16x16x32_f16 v[52:55], v[84:87], v[40:43], v[52:55]
	v_mfma_f32_16x16x32_f16 v[16:19], v[102:105], v[40:43], v[16:19]
	v_mfma_f32_16x16x32_f16 v[20:23], v[32:35], v[8:11], v[20:23]
	v_mfma_f32_16x16x32_f16 v[12:15], v[92:95], v[8:11], v[12:15]
	v_mfma_f32_16x16x32_f16 v[36:39], v[84:87], v[8:11], v[36:39]
	v_mfma_f32_16x16x32_f16 v[4:7], v[102:105], v[8:11], v[4:7]
	v_mad_i64_i32 v[96:97], s[2:3], v140, s12, 0
	v_lshl_add_u64 v[96:97], v[96:97], 2, s[8:9]
	v_lshl_add_u64 v[96:97], v[96:97], 0, v[138:139]
	v_or_b32_e32 v141, 16, v140
	v_mad_i64_i32 v[142:143], s[2:3], v141, s12, 0
	v_lshl_add_u64 v[142:143], v[142:143], 2, s[8:9]
	v_lshl_add_u64 v[142:143], v[142:143], 0, v[138:139]
	v_or_b32_e32 v141, 32, v140
	v_mad_i64_i32 v[144:145], s[2:3], v141, s12, 0
	v_lshl_add_u64 v[144:145], v[144:145], 2, s[8:9]
	v_lshl_add_u64 v[144:145], v[144:145], 0, v[138:139]
	v_or_b32_e32 v141, 48, v140
	v_mad_i64_i32 v[146:147], s[2:3], v141, s12, 0
	v_lshl_add_u64 v[146:147], v[146:147], 2, s[8:9]
	v_lshl_add_u64 v[146:147], v[146:147], 0, v[138:139]
	v_mfma_f32_16x16x32_f16 v[44:47], v[60:63], v[106:109], v[44:47]
	v_mfma_f32_16x16x32_f16 v[76:79], v[118:121], v[106:109], v[76:79]
	v_mfma_f32_16x16x32_f16 v[80:83], v[98:101], v[106:109], v[80:83]
	v_mfma_f32_16x16x32_f16 v[28:31], v[122:125], v[106:109], v[28:31]
	v_mfma_f32_16x16x32_f16 v[72:75], v[60:63], v[110:113], v[72:75]
	v_mfma_f32_16x16x32_f16 v[68:71], v[118:121], v[110:113], v[68:71]
	v_mfma_f32_16x16x32_f16 v[64:67], v[98:101], v[110:113], v[64:67]
	v_mfma_f32_16x16x32_f16 v[24:27], v[122:125], v[110:113], v[24:27]
	v_mfma_f32_16x16x32_f16 v[56:59], v[60:63], v[114:117], v[56:59]
	v_mfma_f32_16x16x32_f16 v[48:51], v[118:121], v[114:117], v[48:51]
	v_mfma_f32_16x16x32_f16 v[52:55], v[98:101], v[114:117], v[52:55]
	v_mfma_f32_16x16x32_f16 v[16:19], v[122:125], v[114:117], v[16:19]
	v_mfma_f32_16x16x32_f16 v[20:23], v[60:63], v[0:3], v[20:23]
	v_mfma_f32_16x16x32_f16 v[12:15], v[118:121], v[0:3], v[12:15]
	v_mfma_f32_16x16x32_f16 v[36:39], v[98:101], v[0:3], v[36:39]
	v_mfma_f32_16x16x32_f16 v[4:7], v[122:125], v[0:3], v[4:7]
	s_waitcnt vmcnt(0)
	v_pk_fma_f32 v[44:45], s[0:1], v[44:45], v[148:149] op_sel_hi:[0,1,1]
	v_pk_fma_f32 v[46:47], s[0:1], v[46:47], v[150:151] op_sel_hi:[0,1,1]
	v_pk_fma_f32 v[76:77], s[0:1], v[76:77], v[152:153] op_sel_hi:[0,1,1]
	v_pk_fma_f32 v[78:79], s[0:1], v[78:79], v[154:155] op_sel_hi:[0,1,1]
	v_pk_fma_f32 v[80:81], s[0:1], v[80:81], v[156:157] op_sel_hi:[0,1,1]
	v_pk_fma_f32 v[82:83], s[0:1], v[82:83], v[158:159] op_sel_hi:[0,1,1]
	v_pk_fma_f32 v[28:29], s[0:1], v[28:29], v[160:161] op_sel_hi:[0,1,1]
	v_pk_fma_f32 v[30:31], s[0:1], v[30:31], v[162:163] op_sel_hi:[0,1,1]
	s_nop 1
	v_permlane16_swap_b32_e32 v44, v76
	v_permlane16_swap_b32_e32 v45, v77
	v_permlane16_swap_b32_e32 v46, v78
	v_permlane16_swap_b32_e32 v47, v79
	v_permlane16_swap_b32_e32 v80, v28
	v_permlane16_swap_b32_e32 v81, v29
	v_permlane16_swap_b32_e32 v82, v30
	v_permlane16_swap_b32_e32 v83, v31
	v_permlane32_swap_b32_e32 v44, v76
	v_permlane32_swap_b32_e32 v45, v77
	v_permlane32_swap_b32_e32 v46, v78
	v_permlane32_swap_b32_e32 v47, v79
	v_permlane32_swap_b32_e32 v80, v28
	v_permlane32_swap_b32_e32 v81, v29
	v_permlane32_swap_b32_e32 v82, v30
	v_permlane32_swap_b32_e32 v83, v31
	global_store_dwordx4 v[96:97], v[44:47], off sc1
	global_store_dwordx4 v[96:97], v[76:79], off offset:64 sc1
	global_store_dwordx4 v[96:97], v[80:83], off offset:128 sc1
	global_store_dwordx4 v[96:97], v[28:31], off offset:192 sc1
	v_pk_fma_f32 v[72:73], s[0:1], v[72:73], v[148:149] op_sel_hi:[0,1,1]
	v_pk_fma_f32 v[74:75], s[0:1], v[74:75], v[150:151] op_sel_hi:[0,1,1]
	v_pk_fma_f32 v[68:69], s[0:1], v[68:69], v[152:153] op_sel_hi:[0,1,1]
	v_pk_fma_f32 v[70:71], s[0:1], v[70:71], v[154:155] op_sel_hi:[0,1,1]
	v_pk_fma_f32 v[64:65], s[0:1], v[64:65], v[156:157] op_sel_hi:[0,1,1]
	v_pk_fma_f32 v[66:67], s[0:1], v[66:67], v[158:159] op_sel_hi:[0,1,1]
	v_pk_fma_f32 v[24:25], s[0:1], v[24:25], v[160:161] op_sel_hi:[0,1,1]
	v_pk_fma_f32 v[26:27], s[0:1], v[26:27], v[162:163] op_sel_hi:[0,1,1]
	s_nop 1
	v_permlane16_swap_b32_e32 v72, v68
	v_permlane16_swap_b32_e32 v73, v69
	v_permlane16_swap_b32_e32 v74, v70
	v_permlane16_swap_b32_e32 v75, v71
	v_permlane16_swap_b32_e32 v64, v24
	v_permlane16_swap_b32_e32 v65, v25
	v_permlane16_swap_b32_e32 v66, v26
	v_permlane16_swap_b32_e32 v67, v27
	v_permlane32_swap_b32_e32 v72, v68
	v_permlane32_swap_b32_e32 v73, v69
	v_permlane32_swap_b32_e32 v74, v70
	v_permlane32_swap_b32_e32 v75, v71
	v_permlane32_swap_b32_e32 v64, v24
	v_permlane32_swap_b32_e32 v65, v25
	v_permlane32_swap_b32_e32 v66, v26
	v_permlane32_swap_b32_e32 v67, v27
	global_store_dwordx4 v[142:143], v[72:75], off sc1
	global_store_dwordx4 v[142:143], v[68:71], off offset:64 sc1
	global_store_dwordx4 v[142:143], v[64:67], off offset:128 sc1
	global_store_dwordx4 v[142:143], v[24:27], off offset:192 sc1
	v_pk_fma_f32 v[56:57], s[0:1], v[56:57], v[148:149] op_sel_hi:[0,1,1]
	v_pk_fma_f32 v[58:59], s[0:1], v[58:59], v[150:151] op_sel_hi:[0,1,1]
	v_pk_fma_f32 v[48:49], s[0:1], v[48:49], v[152:153] op_sel_hi:[0,1,1]
	v_pk_fma_f32 v[50:51], s[0:1], v[50:51], v[154:155] op_sel_hi:[0,1,1]
	v_pk_fma_f32 v[52:53], s[0:1], v[52:53], v[156:157] op_sel_hi:[0,1,1]
	v_pk_fma_f32 v[54:55], s[0:1], v[54:55], v[158:159] op_sel_hi:[0,1,1]
	v_pk_fma_f32 v[16:17], s[0:1], v[16:17], v[160:161] op_sel_hi:[0,1,1]
	v_pk_fma_f32 v[18:19], s[0:1], v[18:19], v[162:163] op_sel_hi:[0,1,1]
	s_nop 1
	v_permlane16_swap_b32_e32 v56, v48
	v_permlane16_swap_b32_e32 v57, v49
	v_permlane16_swap_b32_e32 v58, v50
	v_permlane16_swap_b32_e32 v59, v51
	v_permlane16_swap_b32_e32 v52, v16
	v_permlane16_swap_b32_e32 v53, v17
	v_permlane16_swap_b32_e32 v54, v18
	v_permlane16_swap_b32_e32 v55, v19
	v_permlane32_swap_b32_e32 v56, v48
	v_permlane32_swap_b32_e32 v57, v49
	v_permlane32_swap_b32_e32 v58, v50
	v_permlane32_swap_b32_e32 v59, v51
	v_permlane32_swap_b32_e32 v52, v16
	v_permlane32_swap_b32_e32 v53, v17
	v_permlane32_swap_b32_e32 v54, v18
	v_permlane32_swap_b32_e32 v55, v19
	global_store_dwordx4 v[144:145], v[56:59], off sc1
	global_store_dwordx4 v[144:145], v[48:51], off offset:64 sc1
	global_store_dwordx4 v[144:145], v[52:55], off offset:128 sc1
	global_store_dwordx4 v[144:145], v[16:19], off offset:192 sc1
	v_pk_fma_f32 v[20:21], s[0:1], v[20:21], v[148:149] op_sel_hi:[0,1,1]
	v_pk_fma_f32 v[22:23], s[0:1], v[22:23], v[150:151] op_sel_hi:[0,1,1]
	v_pk_fma_f32 v[12:13], s[0:1], v[12:13], v[152:153] op_sel_hi:[0,1,1]
	v_pk_fma_f32 v[14:15], s[0:1], v[14:15], v[154:155] op_sel_hi:[0,1,1]
	v_pk_fma_f32 v[36:37], s[0:1], v[36:37], v[156:157] op_sel_hi:[0,1,1]
	v_pk_fma_f32 v[38:39], s[0:1], v[38:39], v[158:159] op_sel_hi:[0,1,1]
	v_pk_fma_f32 v[4:5], s[0:1], v[4:5], v[160:161] op_sel_hi:[0,1,1]
	v_pk_fma_f32 v[6:7], s[0:1], v[6:7], v[162:163] op_sel_hi:[0,1,1]
	s_nop 1
	v_permlane16_swap_b32_e32 v20, v12
	v_permlane16_swap_b32_e32 v21, v13
	v_permlane16_swap_b32_e32 v22, v14
	v_permlane16_swap_b32_e32 v23, v15
	v_permlane16_swap_b32_e32 v36, v4
	v_permlane16_swap_b32_e32 v37, v5
	v_permlane16_swap_b32_e32 v38, v6
	v_permlane16_swap_b32_e32 v39, v7
	v_permlane32_swap_b32_e32 v20, v12
	v_permlane32_swap_b32_e32 v21, v13
	v_permlane32_swap_b32_e32 v22, v14
	v_permlane32_swap_b32_e32 v23, v15
	v_permlane32_swap_b32_e32 v36, v4
	v_permlane32_swap_b32_e32 v37, v5
	v_permlane32_swap_b32_e32 v38, v6
	v_permlane32_swap_b32_e32 v39, v7
	global_store_dwordx4 v[146:147], v[20:23], off sc1
	global_store_dwordx4 v[146:147], v[12:15], off offset:64 sc1
	global_store_dwordx4 v[146:147], v[36:39], off offset:128 sc1
	global_store_dwordx4 v[146:147], v[4:7], off offset:192 sc1
	s_endpgm

	.amdhsa_kernel _ZN2g34gemmILi4ELi1EEEvPKDF16_S2_PvPKfiiff
		.amdhsa_group_segment_fixed_size 98304
		.amdhsa_private_segment_fixed_size 0
		.amdhsa_kernarg_size 48
		.amdhsa_user_sgpr_count 2
		.amdhsa_user_sgpr_dispatch_ptr 0
		.amdhsa_user_sgpr_queue_ptr 0
		.amdhsa_user_sgpr_kernarg_segment_ptr 1
		.amdhsa_user_sgpr_dispatch_id 0
		.amdhsa_user_sgpr_kernarg_preload_length 0
		.amdhsa_user_sgpr_kernarg_preload_offset 0
		.amdhsa_user_sgpr_private_segment_size 0
		.amdhsa_uses_dynamic_stack 0
		.amdhsa_enable_private_segment 0
		.amdhsa_system_sgpr_workgroup_id_x 1
		.amdhsa_system_sgpr_workgroup_id_y 0
		.amdhsa_system_sgpr_workgroup_id_z 0
		.amdhsa_system_sgpr_workgroup_info 0
		.amdhsa_system_vgpr_workitem_id 0
		.amdhsa_next_free_vgpr 169
		.amdhsa_next_free_sgpr 96
		.amdhsa_accum_offset 168
		.amdhsa_reserve_vcc 0
		.amdhsa_float_round_mode_32 0
		.amdhsa_float_round_mode_16_64 0
		.amdhsa_float_denorm_mode_32 3
		.amdhsa_float_denorm_mode_16_64 3
		.amdhsa_dx10_clamp 1
		.amdhsa_ieee_mode 1
		.amdhsa_fp16_overflow 0
		.amdhsa_tg_split 0
		.amdhsa_exception_fp_ieee_invalid_op 0
		.amdhsa_exception_fp_denorm_src 0
		.amdhsa_exception_fp_ieee_div_zero 0
		.amdhsa_exception_fp_ieee_overflow 0
		.amdhsa_exception_fp_ieee_underflow 0
		.amdhsa_exception_fp_ieee_inexact 0
		.amdhsa_exception_int_div_zero 0
	.end_amdhsa_kernel
